# accumulator clears at GEMM unit headers: 64-bit moves (64 instead of 128 VALU issues per unit)
# speedup vs baseline: 1.0100x; 1.0100x over previous
.LBB0_290:
	s_ashr_i32 s15, s14, 31
	s_lshl_b64 s[16:17], s[14:15], 19
	v_readlane_b32 s20, v254, 49
	v_readlane_b32 s21, v254, 50
	s_add_u32 s16, s20, s16
	s_addc_u32 s17, s21, s17
	s_and_b64 s[20:21], s[18:19], exec
	s_cselect_b32 s15, s17, s25
	s_cselect_b32 s23, s16, s24
	s_ashr_i32 s13, s12, 31
	s_lshl_b64 s[20:21], s[12:13], 19
	s_add_u32 s20, s4, s20
	s_addc_u32 s21, s5, s21
	s_and_b64 s[34:35], s[18:19], exec
	s_cselect_b32 s13, s21, s29
	s_cselect_b32 s60, s20, s28
	s_cmp_eq_u32 s30, 0
	s_cselect_b32 s61, -2, 0
	s_add_u32 s63, s28, 0x10000
	s_mov_b32 s62, 0
	s_addc_u32 s64, s29, 0
	v_lshl_add_u64 v[210:211], s[24:25], 0, v[204:205]
	v_lshl_add_u64 v[212:213], s[24:25], 0, v[206:207]
	v_mov_b64_e32 v[2:3], 0
	v_mov_b64_e32 v[4:5], 0
	v_mov_b64_e32 v[6:7], 0
	v_mov_b64_e32 v[8:9], 0
	v_mov_b64_e32 v[10:11], 0
	v_mov_b64_e32 v[12:13], 0
	v_mov_b64_e32 v[14:15], 0
	v_mov_b64_e32 v[16:17], 0
	v_mov_b64_e32 v[18:19], 0
	v_mov_b64_e32 v[20:21], 0
	v_mov_b64_e32 v[22:23], 0
	v_mov_b64_e32 v[24:25], 0
	v_mov_b64_e32 v[26:27], 0
	v_mov_b64_e32 v[28:29], 0
	v_mov_b64_e32 v[30:31], 0
	v_mov_b64_e32 v[32:33], 0
	v_mov_b64_e32 v[34:35], 0
	v_mov_b64_e32 v[36:37], 0
	v_mov_b64_e32 v[38:39], 0
	v_mov_b64_e32 v[40:41], 0
	v_mov_b64_e32 v[42:43], 0
	v_mov_b64_e32 v[44:45], 0
	v_mov_b64_e32 v[46:47], 0
	v_mov_b64_e32 v[48:49], 0
	v_mov_b64_e32 v[50:51], 0
	v_mov_b64_e32 v[52:53], 0
	v_mov_b64_e32 v[54:55], 0
	v_mov_b64_e32 v[56:57], 0
	v_mov_b64_e32 v[58:59], 0
	v_mov_b64_e32 v[60:61], 0
	v_mov_b64_e32 v[62:63], 0
	v_mov_b64_e32 v[64:65], 0
	v_mov_b64_e32 v[66:67], 0
	v_mov_b64_e32 v[68:69], 0
	v_mov_b64_e32 v[70:71], 0
	v_mov_b64_e32 v[72:73], 0
	v_mov_b64_e32 v[74:75], 0
	v_mov_b64_e32 v[76:77], 0
	v_mov_b64_e32 v[78:79], 0
	v_mov_b64_e32 v[80:81], 0
	v_mov_b64_e32 v[82:83], 0
	v_mov_b64_e32 v[84:85], 0
	v_mov_b64_e32 v[86:87], 0
	v_mov_b64_e32 v[88:89], 0
	v_mov_b64_e32 v[90:91], 0
	v_mov_b64_e32 v[92:93], 0
	v_mov_b64_e32 v[94:95], 0
	v_mov_b64_e32 v[96:97], 0
	v_mov_b64_e32 v[98:99], 0
	v_mov_b64_e32 v[100:101], 0
	v_mov_b64_e32 v[102:103], 0
	v_mov_b64_e32 v[104:105], 0
	v_mov_b64_e32 v[106:107], 0
	v_mov_b64_e32 v[108:109], 0
	v_mov_b64_e32 v[110:111], 0
	v_mov_b64_e32 v[112:113], 0
	v_mov_b64_e32 v[114:115], 0
	v_mov_b64_e32 v[116:117], 0
	v_mov_b64_e32 v[118:119], 0
	v_mov_b64_e32 v[120:121], 0
	v_mov_b64_e32 v[122:123], 0
	v_mov_b64_e32 v[124:125], 0
	v_mov_b64_e32 v[126:127], 0
	v_mov_b64_e32 v[128:129], 0
	s_waitcnt lgkmcnt(0)
	s_branch .LBB0_292

.LBB0_591:
	s_ashr_i32 s15, s14, 31
	s_lshl_b64 s[16:17], s[14:15], 19
	v_readlane_b32 s20, v254, 49
	v_readlane_b32 s21, v254, 50
	s_add_u32 s16, s20, s16
	s_addc_u32 s17, s21, s17
	s_and_b64 s[20:21], s[18:19], exec
	s_cselect_b32 s15, s17, s27
	s_cselect_b32 s25, s16, s26
	s_ashr_i32 s13, s12, 31
	s_lshl_b64 s[20:21], s[12:13], 19
	s_add_u32 s20, s4, s20
	s_addc_u32 s21, s5, s21
	s_and_b64 s[36:37], s[18:19], exec
	s_cselect_b32 s13, s21, s31
	s_cselect_b32 s60, s20, s30
	s_cmp_eq_u32 s34, 0
	s_cselect_b32 s61, -2, 0
	s_add_u32 s63, s30, 0x10000
	s_mov_b32 s62, 0
	s_addc_u32 s64, s31, 0
	v_lshl_add_u64 v[210:211], s[26:27], 0, v[204:205]
	v_lshl_add_u64 v[212:213], s[26:27], 0, v[206:207]
	v_mov_b64_e32 v[2:3], 0
	v_mov_b64_e32 v[4:5], 0
	v_mov_b64_e32 v[6:7], 0
	v_mov_b64_e32 v[8:9], 0
	v_mov_b64_e32 v[10:11], 0
	v_mov_b64_e32 v[12:13], 0
	v_mov_b64_e32 v[14:15], 0
	v_mov_b64_e32 v[16:17], 0
	v_mov_b64_e32 v[18:19], 0
	v_mov_b64_e32 v[20:21], 0
	v_mov_b64_e32 v[22:23], 0
	v_mov_b64_e32 v[24:25], 0
	v_mov_b64_e32 v[26:27], 0
	v_mov_b64_e32 v[28:29], 0
	v_mov_b64_e32 v[30:31], 0
	v_mov_b64_e32 v[32:33], 0
	v_mov_b64_e32 v[34:35], 0
	v_mov_b64_e32 v[36:37], 0
	v_mov_b64_e32 v[38:39], 0
	v_mov_b64_e32 v[40:41], 0
	v_mov_b64_e32 v[42:43], 0
	v_mov_b64_e32 v[44:45], 0
	v_mov_b64_e32 v[46:47], 0
	v_mov_b64_e32 v[48:49], 0
	v_mov_b64_e32 v[50:51], 0
	v_mov_b64_e32 v[52:53], 0
	v_mov_b64_e32 v[54:55], 0
	v_mov_b64_e32 v[56:57], 0
	v_mov_b64_e32 v[58:59], 0
	v_mov_b64_e32 v[60:61], 0
	v_mov_b64_e32 v[62:63], 0
	v_mov_b64_e32 v[64:65], 0
	v_mov_b64_e32 v[66:67], 0
	v_mov_b64_e32 v[68:69], 0
	v_mov_b64_e32 v[70:71], 0
	v_mov_b64_e32 v[72:73], 0
	v_mov_b64_e32 v[74:75], 0
	v_mov_b64_e32 v[76:77], 0
	v_mov_b64_e32 v[78:79], 0
	v_mov_b64_e32 v[80:81], 0
	v_mov_b64_e32 v[82:83], 0
	v_mov_b64_e32 v[84:85], 0
	v_mov_b64_e32 v[86:87], 0
	v_mov_b64_e32 v[88:89], 0
	v_mov_b64_e32 v[90:91], 0
	v_mov_b64_e32 v[92:93], 0
	v_mov_b64_e32 v[94:95], 0
	v_mov_b64_e32 v[96:97], 0
	v_mov_b64_e32 v[98:99], 0
	v_mov_b64_e32 v[100:101], 0
	v_mov_b64_e32 v[102:103], 0
	v_mov_b64_e32 v[104:105], 0
	v_mov_b64_e32 v[106:107], 0
	v_mov_b64_e32 v[108:109], 0
	v_mov_b64_e32 v[110:111], 0
	v_mov_b64_e32 v[112:113], 0
	v_mov_b64_e32 v[114:115], 0
	v_mov_b64_e32 v[116:117], 0
	v_mov_b64_e32 v[118:119], 0
	v_mov_b64_e32 v[120:121], 0
	v_mov_b64_e32 v[122:123], 0
	v_mov_b64_e32 v[124:125], 0
	v_mov_b64_e32 v[126:127], 0
	v_mov_b64_e32 v[128:129], 0
	s_branch .LBB0_593

.LBB0_749:
	s_add_i32 s51, s28, 1
	s_cmp_lt_u32 s51, s45
	s_cselect_b64 s[4:5], -1, 0
	s_and_b64 s[26:27], s[4:5], s[0:1]
	s_ashr_i32 s15, s14, 31
	s_andn2_b64 vcc, exec, s[26:27]
	s_lshl_b64 s[16:17], s[14:15], 20
	s_add_u32 s16, s33, s16
	s_addc_u32 s17, s42, s17
	s_and_b64 s[18:19], s[26:27], exec
	s_cselect_b32 s15, s17, s23
	s_cselect_b32 s52, s16, s22
	s_ashr_i32 s13, s12, 31
	s_lshl_b64 s[18:19], s[12:13], 20
	s_add_u32 s18, s6, s18
	s_addc_u32 s19, s7, s19
	v_cndmask_b32_e64 v2, 0, 1, s[26:27]
	s_and_b64 s[26:27], s[26:27], exec
	s_cselect_b32 s13, s19, s25
	s_cselect_b32 s53, s18, s24
	s_cmp_eq_u32 s28, 0
	v_cmp_ne_u32_e64 s[4:5], 1, v2
	s_cselect_b32 s54, -2, 0
	s_add_u32 s56, s24, 0x10000
	v_mov_b32_e32 v2, 0
	s_mov_b32 s55, 0
	s_addc_u32 s57, s25, 0
	v_lshl_add_u64 v[206:207], s[22:23], 0, v[202:203]
	v_lshl_add_u64 v[208:209], s[22:23], 0, v[204:205]
	s_mov_b64 s[24:25], 0
	v_mov_b32_e32 v3, 0
	v_mov_b64_e32 v[4:5], 0
	v_mov_b64_e32 v[6:7], 0
	v_mov_b64_e32 v[8:9], 0
	v_mov_b64_e32 v[10:11], 0
	v_mov_b64_e32 v[12:13], 0
	v_mov_b64_e32 v[14:15], 0
	v_mov_b64_e32 v[16:17], 0
	v_mov_b64_e32 v[18:19], 0
	v_mov_b64_e32 v[20:21], 0
	v_mov_b64_e32 v[22:23], 0
	v_mov_b64_e32 v[24:25], 0
	v_mov_b64_e32 v[26:27], 0
	v_mov_b64_e32 v[28:29], 0
	v_mov_b64_e32 v[30:31], 0
	v_mov_b64_e32 v[32:33], 0
	v_mov_b64_e32 v[34:35], 0
	v_mov_b64_e32 v[36:37], 0
	v_mov_b64_e32 v[38:39], 0
	v_mov_b64_e32 v[40:41], 0
	v_mov_b64_e32 v[42:43], 0
	v_mov_b64_e32 v[44:45], 0
	v_mov_b64_e32 v[46:47], 0
	v_mov_b64_e32 v[48:49], 0
	v_mov_b64_e32 v[50:51], 0
	v_mov_b64_e32 v[52:53], 0
	v_mov_b64_e32 v[54:55], 0
	v_mov_b64_e32 v[56:57], 0
	v_mov_b64_e32 v[58:59], 0
	v_mov_b64_e32 v[60:61], 0
	v_mov_b64_e32 v[62:63], 0
	v_mov_b64_e32 v[64:65], 0
	v_mov_b64_e32 v[82:83], 0
	v_mov_b64_e32 v[84:85], 0
	v_mov_b64_e32 v[86:87], 0
	v_mov_b64_e32 v[88:89], 0
	v_mov_b64_e32 v[90:91], 0
	v_mov_b64_e32 v[92:93], 0
	v_mov_b64_e32 v[94:95], 0
	v_mov_b64_e32 v[96:97], 0
	v_mov_b64_e32 v[98:99], 0
	v_mov_b64_e32 v[100:101], 0
	v_mov_b64_e32 v[102:103], 0
	v_mov_b64_e32 v[104:105], 0
	v_mov_b64_e32 v[106:107], 0
	v_mov_b64_e32 v[108:109], 0
	v_mov_b64_e32 v[110:111], 0
	v_mov_b64_e32 v[112:113], 0
	v_mov_b64_e32 v[114:115], 0
	v_mov_b64_e32 v[116:117], 0
	v_mov_b64_e32 v[118:119], 0
	v_mov_b64_e32 v[120:121], 0
	v_mov_b64_e32 v[122:123], 0
	v_mov_b64_e32 v[124:125], 0
	v_mov_b64_e32 v[126:127], 0
	v_mov_b64_e32 v[128:129], 0
	v_mov_b64_e32 v[130:131], 0
	v_mov_b64_e32 v[132:133], 0
	v_mov_b64_e32 v[134:135], 0
	v_mov_b64_e32 v[136:137], 0
	v_mov_b64_e32 v[138:139], 0
	v_mov_b64_e32 v[140:141], 0
	v_mov_b64_e32 v[142:143], 0
	v_mov_b64_e32 v[144:145], 0
	s_waitcnt lgkmcnt(0)
	s_branch .LBB0_751

.LBB0_1050:
	s_ashr_i32 s11, s10, 31
	s_lshl_b64 s[12:13], s[10:11], 20
	s_add_u32 s12, s33, s12
	s_addc_u32 s13, s42, s13
	s_and_b64 s[16:17], s[14:15], exec
	s_cselect_b32 s11, s13, s23
	s_cselect_b32 s19, s12, s22
	s_ashr_i32 s9, s8, 31
	s_lshl_b64 s[16:17], s[8:9], 20
	s_add_u32 s16, s6, s16
	s_addc_u32 s17, s7, s17
	s_and_b64 s[30:31], s[14:15], exec
	s_cselect_b32 s9, s17, s27
	s_cselect_b32 s53, s16, s26
	s_cmp_eq_u32 s28, 0
	s_cselect_b32 s54, -2, 0
	s_add_u32 s56, s26, 0x10000
	v_mov_b32_e32 v2, 0
	s_mov_b32 s55, 0
	s_addc_u32 s57, s27, 0
	v_lshl_add_u64 v[208:209], s[22:23], 0, v[202:203]
	v_lshl_add_u64 v[210:211], s[22:23], 0, v[204:205]
	v_mov_b32_e32 v3, 0
	v_mov_b64_e32 v[4:5], 0
	v_mov_b64_e32 v[6:7], 0
	v_mov_b64_e32 v[8:9], 0
	v_mov_b64_e32 v[10:11], 0
	v_mov_b64_e32 v[12:13], 0
	v_mov_b64_e32 v[14:15], 0
	v_mov_b64_e32 v[16:17], 0
	v_mov_b64_e32 v[18:19], 0
	v_mov_b64_e32 v[20:21], 0
	v_mov_b64_e32 v[22:23], 0
	v_mov_b64_e32 v[24:25], 0
	v_mov_b64_e32 v[26:27], 0
	v_mov_b64_e32 v[28:29], 0
	v_mov_b64_e32 v[30:31], 0
	v_mov_b64_e32 v[32:33], 0
	v_mov_b64_e32 v[34:35], 0
	v_mov_b64_e32 v[36:37], 0
	v_mov_b64_e32 v[38:39], 0
	v_mov_b64_e32 v[40:41], 0
	v_mov_b64_e32 v[42:43], 0
	v_mov_b64_e32 v[44:45], 0
	v_mov_b64_e32 v[46:47], 0
	v_mov_b64_e32 v[48:49], 0
	v_mov_b64_e32 v[50:51], 0
	v_mov_b64_e32 v[52:53], 0
	v_mov_b64_e32 v[54:55], 0
	v_mov_b64_e32 v[56:57], 0
	v_mov_b64_e32 v[58:59], 0
	v_mov_b64_e32 v[60:61], 0
	v_mov_b64_e32 v[62:63], 0
	v_mov_b64_e32 v[64:65], 0
	v_mov_b64_e32 v[82:83], 0
	v_mov_b64_e32 v[84:85], 0
	v_mov_b64_e32 v[86:87], 0
	v_mov_b64_e32 v[88:89], 0
	v_mov_b64_e32 v[90:91], 0
	v_mov_b64_e32 v[92:93], 0
	v_mov_b64_e32 v[94:95], 0
	v_mov_b64_e32 v[96:97], 0
	v_mov_b64_e32 v[98:99], 0
	v_mov_b64_e32 v[100:101], 0
	v_mov_b64_e32 v[102:103], 0
	v_mov_b64_e32 v[104:105], 0
	v_mov_b64_e32 v[106:107], 0
	v_mov_b64_e32 v[108:109], 0
	v_mov_b64_e32 v[110:111], 0
	v_mov_b64_e32 v[112:113], 0
	v_mov_b64_e32 v[114:115], 0
	v_mov_b64_e32 v[116:117], 0
	v_mov_b64_e32 v[118:119], 0
	v_mov_b64_e32 v[120:121], 0
	v_mov_b64_e32 v[122:123], 0
	v_mov_b64_e32 v[124:125], 0
	v_mov_b64_e32 v[126:127], 0
	v_mov_b64_e32 v[128:129], 0
	v_mov_b64_e32 v[130:131], 0
	v_mov_b64_e32 v[132:133], 0
	v_mov_b64_e32 v[134:135], 0
	v_mov_b64_e32 v[136:137], 0
	v_mov_b64_e32 v[138:139], 0
	v_mov_b64_e32 v[140:141], 0
	v_mov_b64_e32 v[142:143], 0
	v_mov_b64_e32 v[144:145], 0
	s_branch .LBB0_1052

.LBB0_1183:
	s_ashr_i32 s11, s10, 31
	s_lshl_b64 s[12:13], s[10:11], 19
	v_readlane_b32 s16, v254, 49
	v_readlane_b32 s17, v254, 50
	s_add_u32 s12, s16, s12
	s_addc_u32 s13, s17, s13
	s_and_b64 s[16:17], s[14:15], exec
	s_cselect_b32 s11, s13, s21
	s_cselect_b32 s56, s12, s20
	s_ashr_i32 s9, s8, 31
	s_lshl_b64 s[16:17], s[8:9], 19
	s_add_u32 s16, s6, s16
	s_addc_u32 s17, s7, s17
	s_and_b64 s[28:29], s[14:15], exec
	s_cselect_b32 s9, s17, s25
	s_cselect_b32 s57, s16, s24
	s_cmp_eq_u32 s26, 0
	s_cselect_b32 s58, -2, 0
	s_add_u32 s60, s24, 0x10000
	s_mov_b32 s59, 0
	s_addc_u32 s61, s25, 0
	v_lshl_add_u64 v[236:237], s[20:21], 0, v[232:233]
	v_lshl_add_u64 v[238:239], s[20:21], 0, v[234:235]
	v_mov_b64_e32 v[2:3], 0
	v_mov_b64_e32 v[4:5], 0
	v_mov_b64_e32 v[6:7], 0
	v_mov_b64_e32 v[8:9], 0
	v_mov_b64_e32 v[10:11], 0
	v_mov_b64_e32 v[12:13], 0
	v_mov_b64_e32 v[14:15], 0
	v_mov_b64_e32 v[16:17], 0
	v_mov_b64_e32 v[18:19], 0
	v_mov_b64_e32 v[20:21], 0
	v_mov_b64_e32 v[22:23], 0
	v_mov_b64_e32 v[24:25], 0
	v_mov_b64_e32 v[26:27], 0
	v_mov_b64_e32 v[28:29], 0
	v_mov_b64_e32 v[30:31], 0
	v_mov_b64_e32 v[32:33], 0
	v_mov_b64_e32 v[34:35], 0
	v_mov_b64_e32 v[36:37], 0
	v_mov_b64_e32 v[38:39], 0
	v_mov_b64_e32 v[40:41], 0
	v_mov_b64_e32 v[42:43], 0
	v_mov_b64_e32 v[44:45], 0
	v_mov_b64_e32 v[46:47], 0
	v_mov_b64_e32 v[48:49], 0
	v_mov_b64_e32 v[50:51], 0
	v_mov_b64_e32 v[52:53], 0
	v_mov_b64_e32 v[54:55], 0
	v_mov_b64_e32 v[56:57], 0
	v_mov_b64_e32 v[58:59], 0
	v_mov_b64_e32 v[60:61], 0
	v_mov_b64_e32 v[62:63], 0
	v_mov_b64_e32 v[64:65], 0
	v_mov_b64_e32 v[66:67], 0
	v_mov_b64_e32 v[68:69], 0
	v_mov_b64_e32 v[70:71], 0
	v_mov_b64_e32 v[72:73], 0
	v_mov_b64_e32 v[74:75], 0
	v_mov_b64_e32 v[76:77], 0
	v_mov_b64_e32 v[78:79], 0
	v_mov_b64_e32 v[80:81], 0
	v_mov_b64_e32 v[82:83], 0
	v_mov_b64_e32 v[84:85], 0
	v_mov_b64_e32 v[86:87], 0
	v_mov_b64_e32 v[88:89], 0
	v_mov_b64_e32 v[90:91], 0
	v_mov_b64_e32 v[92:93], 0
	v_mov_b64_e32 v[94:95], 0
	v_mov_b64_e32 v[96:97], 0
	v_mov_b64_e32 v[98:99], 0
	v_mov_b64_e32 v[100:101], 0
	v_mov_b64_e32 v[102:103], 0
	v_mov_b64_e32 v[104:105], 0
	v_mov_b64_e32 v[106:107], 0
	v_mov_b64_e32 v[108:109], 0
	v_mov_b64_e32 v[110:111], 0
	v_mov_b64_e32 v[112:113], 0
	v_mov_b64_e32 v[114:115], 0
	v_mov_b64_e32 v[116:117], 0
	v_mov_b64_e32 v[118:119], 0
	v_mov_b64_e32 v[120:121], 0
	v_mov_b64_e32 v[122:123], 0
	v_mov_b64_e32 v[124:125], 0
	v_mov_b64_e32 v[126:127], 0
	v_mov_b64_e32 v[128:129], 0
	s_waitcnt lgkmcnt(0)
	s_branch .LBB0_1185

.LBB0_1503:
	s_ashr_i32 s11, s10, 31
	s_lshl_b64 s[12:13], s[10:11], 19
	v_readlane_b32 s16, v254, 49
	v_readlane_b32 s17, v254, 50
	s_add_u32 s12, s16, s12
	s_addc_u32 s13, s17, s13
	s_and_b64 s[16:17], s[14:15], exec
	s_cselect_b32 s11, s13, s23
	s_cselect_b32 s19, s12, s22
	s_ashr_i32 s9, s8, 31
	s_lshl_b64 s[16:17], s[8:9], 19
	s_add_u32 s16, s6, s16
	s_addc_u32 s17, s7, s17
	s_and_b64 s[30:31], s[14:15], exec
	s_cselect_b32 s9, s17, s27
	s_cselect_b32 s21, s16, s26
	s_cmp_eq_u32 s28, 0
	s_cselect_b32 s58, -2, 0
	s_add_u32 s60, s26, 0x10000
	s_mov_b32 s59, 0
	s_addc_u32 s61, s27, 0
	v_lshl_add_u64 v[238:239], s[22:23], 0, v[232:233]
	v_lshl_add_u64 v[240:241], s[22:23], 0, v[234:235]
	v_mov_b64_e32 v[2:3], 0
	v_mov_b64_e32 v[4:5], 0
	v_mov_b64_e32 v[6:7], 0
	v_mov_b64_e32 v[8:9], 0
	v_mov_b64_e32 v[10:11], 0
	v_mov_b64_e32 v[12:13], 0
	v_mov_b64_e32 v[14:15], 0
	v_mov_b64_e32 v[16:17], 0
	v_mov_b64_e32 v[18:19], 0
	v_mov_b64_e32 v[20:21], 0
	v_mov_b64_e32 v[22:23], 0
	v_mov_b64_e32 v[24:25], 0
	v_mov_b64_e32 v[26:27], 0
	v_mov_b64_e32 v[28:29], 0
	v_mov_b64_e32 v[30:31], 0
	v_mov_b64_e32 v[32:33], 0
	v_mov_b64_e32 v[34:35], 0
	v_mov_b64_e32 v[36:37], 0
	v_mov_b64_e32 v[38:39], 0
	v_mov_b64_e32 v[40:41], 0
	v_mov_b64_e32 v[42:43], 0
	v_mov_b64_e32 v[44:45], 0
	v_mov_b64_e32 v[46:47], 0
	v_mov_b64_e32 v[48:49], 0
	v_mov_b64_e32 v[50:51], 0
	v_mov_b64_e32 v[52:53], 0
	v_mov_b64_e32 v[54:55], 0
	v_mov_b64_e32 v[56:57], 0
	v_mov_b64_e32 v[58:59], 0
	v_mov_b64_e32 v[60:61], 0
	v_mov_b64_e32 v[62:63], 0
	v_mov_b64_e32 v[64:65], 0
	v_mov_b64_e32 v[66:67], 0
	v_mov_b64_e32 v[68:69], 0
	v_mov_b64_e32 v[70:71], 0
	v_mov_b64_e32 v[72:73], 0
	v_mov_b64_e32 v[74:75], 0
	v_mov_b64_e32 v[76:77], 0
	v_mov_b64_e32 v[78:79], 0
	v_mov_b64_e32 v[80:81], 0
	v_mov_b64_e32 v[82:83], 0
	v_mov_b64_e32 v[84:85], 0
	v_mov_b64_e32 v[86:87], 0
	v_mov_b64_e32 v[88:89], 0
	v_mov_b64_e32 v[90:91], 0
	v_mov_b64_e32 v[92:93], 0
	v_mov_b64_e32 v[94:95], 0
	v_mov_b64_e32 v[96:97], 0
	v_mov_b64_e32 v[98:99], 0
	v_mov_b64_e32 v[100:101], 0
	v_mov_b64_e32 v[102:103], 0
	v_mov_b64_e32 v[104:105], 0
	v_mov_b64_e32 v[106:107], 0
	v_mov_b64_e32 v[108:109], 0
	v_mov_b64_e32 v[110:111], 0
	v_mov_b64_e32 v[112:113], 0
	v_mov_b64_e32 v[114:115], 0
	v_mov_b64_e32 v[116:117], 0
	v_mov_b64_e32 v[118:119], 0
	v_mov_b64_e32 v[120:121], 0
	v_mov_b64_e32 v[122:123], 0
	v_mov_b64_e32 v[124:125], 0
	v_mov_b64_e32 v[126:127], 0
	v_mov_b64_e32 v[128:129], 0
	s_branch .LBB0_1505

.LBB0_1586:
	s_cmp_eq_u32 s20, 0
	s_cselect_b32 s49, -2, 0
	s_add_u32 s51, s18, 0x10000
	v_mov_b32_e32 v66, 0
	s_mov_b32 s50, 0
	s_addc_u32 s52, s19, 0
	v_lshl_add_u64 v[206:207], s[16:17], 0, v[202:203]
	v_lshl_add_u64 v[208:209], s[16:17], 0, v[204:205]
	s_mov_b64 s[18:19], 0
	v_mov_b32_e32 v67, 0
	v_mov_b64_e32 v[68:69], 0
	v_mov_b64_e32 v[70:71], 0
	v_mov_b64_e32 v[72:73], 0
	v_mov_b64_e32 v[74:75], 0
	v_mov_b64_e32 v[76:77], 0
	s_waitcnt lgkmcnt(0)
	v_mov_b64_e32 v[78:79], 0
	v_mov_b64_e32 v[80:81], 0
	v_mov_b64_e32 v[82:83], 0
	v_mov_b64_e32 v[84:85], 0
	v_mov_b64_e32 v[86:87], 0
	v_mov_b64_e32 v[88:89], 0
	v_mov_b64_e32 v[90:91], 0
	v_mov_b64_e32 v[92:93], 0
	v_mov_b64_e32 v[94:95], 0
	v_mov_b64_e32 v[96:97], 0
	v_mov_b64_e32 v[98:99], 0
	v_mov_b64_e32 v[100:101], 0
	v_mov_b64_e32 v[102:103], 0
	v_mov_b64_e32 v[104:105], 0
	v_mov_b64_e32 v[106:107], 0
	v_mov_b64_e32 v[108:109], 0
	v_mov_b64_e32 v[110:111], 0
	v_mov_b64_e32 v[112:113], 0
	v_mov_b64_e32 v[114:115], 0
	v_mov_b64_e32 v[116:117], 0
	v_mov_b64_e32 v[118:119], 0
	v_mov_b64_e32 v[120:121], 0
	v_mov_b64_e32 v[122:123], 0
	v_mov_b64_e32 v[124:125], 0
	v_mov_b64_e32 v[126:127], 0
	v_mov_b64_e32 v[128:129], 0
	v_mov_b64_e32 v[130:131], 0
	v_mov_b64_e32 v[132:133], 0
	v_mov_b64_e32 v[134:135], 0
	v_mov_b64_e32 v[136:137], 0
	v_mov_b64_e32 v[138:139], 0
	v_mov_b64_e32 v[140:141], 0
	v_mov_b64_e32 v[142:143], 0
	v_mov_b64_e32 v[144:145], 0
	v_mov_b64_e32 v[146:147], 0
	v_mov_b64_e32 v[148:149], 0
	v_mov_b64_e32 v[150:151], 0
	v_mov_b64_e32 v[152:153], 0
	v_mov_b64_e32 v[154:155], 0
	v_mov_b64_e32 v[156:157], 0
	v_mov_b64_e32 v[158:159], 0
	v_mov_b64_e32 v[160:161], 0
	v_mov_b64_e32 v[162:163], 0
	v_mov_b64_e32 v[164:165], 0
	v_mov_b64_e32 v[166:167], 0
	v_mov_b64_e32 v[168:169], 0
	v_mov_b64_e32 v[170:171], 0
	v_mov_b64_e32 v[172:173], 0
	v_mov_b64_e32 v[174:175], 0
	v_mov_b64_e32 v[176:177], 0
	v_mov_b64_e32 v[178:179], 0
	v_mov_b64_e32 v[180:181], 0
	v_mov_b64_e32 v[182:183], 0
	v_mov_b64_e32 v[184:185], 0
	v_mov_b64_e32 v[186:187], 0
	v_mov_b64_e32 v[188:189], 0
	v_mov_b64_e32 v[190:191], 0
	v_mov_b64_e32 v[192:193], 0
	s_branch .LBB0_1588

.LBB0_1939:
	s_cmp_eq_u32 s18, 0
	s_cselect_b32 s49, -2, 0
	s_add_u32 s51, s16, 0x10000
	v_mov_b32_e32 v66, 0
	s_mov_b32 s50, 0
	s_addc_u32 s52, s17, 0
	v_lshl_add_u64 v[208:209], s[14:15], 0, v[202:203]
	v_lshl_add_u64 v[210:211], s[14:15], 0, v[204:205]
	s_mov_b64 s[16:17], 0
	v_mov_b32_e32 v67, 0
	v_mov_b64_e32 v[68:69], 0
	v_mov_b64_e32 v[70:71], 0
	v_mov_b64_e32 v[72:73], 0
	v_mov_b64_e32 v[74:75], 0
	v_mov_b64_e32 v[76:77], 0
	v_mov_b64_e32 v[78:79], 0
	v_mov_b64_e32 v[80:81], 0
	v_mov_b64_e32 v[82:83], 0
	v_mov_b64_e32 v[84:85], 0
	v_mov_b64_e32 v[86:87], 0
	v_mov_b64_e32 v[88:89], 0
	v_mov_b64_e32 v[90:91], 0
	v_mov_b64_e32 v[92:93], 0
	v_mov_b64_e32 v[94:95], 0
	v_mov_b64_e32 v[96:97], 0
	v_mov_b64_e32 v[98:99], 0
	v_mov_b64_e32 v[100:101], 0
	v_mov_b64_e32 v[102:103], 0
	v_mov_b64_e32 v[104:105], 0
	v_mov_b64_e32 v[106:107], 0
	v_mov_b64_e32 v[108:109], 0
	v_mov_b64_e32 v[110:111], 0
	v_mov_b64_e32 v[112:113], 0
	v_mov_b64_e32 v[114:115], 0
	v_mov_b64_e32 v[116:117], 0
	v_mov_b64_e32 v[118:119], 0
	v_mov_b64_e32 v[120:121], 0
	v_mov_b64_e32 v[122:123], 0
	v_mov_b64_e32 v[124:125], 0
	v_mov_b64_e32 v[126:127], 0
	v_mov_b64_e32 v[128:129], 0
	v_mov_b64_e32 v[130:131], 0
	v_mov_b64_e32 v[132:133], 0
	v_mov_b64_e32 v[134:135], 0
	v_mov_b64_e32 v[136:137], 0
	v_mov_b64_e32 v[138:139], 0
	v_mov_b64_e32 v[140:141], 0
	v_mov_b64_e32 v[142:143], 0
	v_mov_b64_e32 v[144:145], 0
	v_mov_b64_e32 v[146:147], 0
	v_mov_b64_e32 v[148:149], 0
	v_mov_b64_e32 v[150:151], 0
	v_mov_b64_e32 v[152:153], 0
	v_mov_b64_e32 v[154:155], 0
	v_mov_b64_e32 v[156:157], 0
	v_mov_b64_e32 v[158:159], 0
	v_mov_b64_e32 v[160:161], 0
	v_mov_b64_e32 v[162:163], 0
	v_mov_b64_e32 v[164:165], 0
	v_mov_b64_e32 v[166:167], 0
	v_mov_b64_e32 v[168:169], 0
	v_mov_b64_e32 v[170:171], 0
	v_mov_b64_e32 v[172:173], 0
	v_mov_b64_e32 v[174:175], 0
	v_mov_b64_e32 v[176:177], 0
	v_mov_b64_e32 v[178:179], 0
	v_mov_b64_e32 v[180:181], 0
	v_mov_b64_e32 v[182:183], 0
	v_mov_b64_e32 v[184:185], 0
	v_mov_b64_e32 v[186:187], 0
	v_mov_b64_e32 v[188:189], 0
	v_mov_b64_e32 v[190:191], 0
	v_mov_b64_e32 v[192:193], 0
	s_branch .LBB0_1941

.LBB0_2077:
	s_ashr_i32 s21, s20, 31
	s_lshl_b64 s[22:23], s[20:21], 19
	v_readlane_b32 s26, v254, 49
	v_readlane_b32 s27, v254, 50
	s_add_u32 s22, s26, s22
	s_addc_u32 s23, s27, s23
	s_and_b64 s[26:27], s[24:25], exec
	s_cselect_b32 s2, s23, s1
	s_cselect_b32 s21, s22, s0
	s_ashr_i32 s19, s18, 31
	s_lshl_b64 s[26:27], s[18:19], 19
	s_add_u32 s26, s4, s26
	s_addc_u32 s27, s5, s27
	s_and_b64 s[40:41], s[24:25], exec
	s_cselect_b32 s19, s27, s37
	s_cselect_b32 s66, s26, s36
	s_cmp_eq_u32 s38, 0
	s_cselect_b32 s67, -2, 0
	s_add_u32 s69, s36, 0x10000
	s_mov_b32 s68, 0
	s_addc_u32 s70, s37, 0
	v_lshl_add_u64 v[210:211], s[0:1], 0, v[204:205]
	v_lshl_add_u64 v[212:213], s[0:1], 0, v[206:207]
	v_mov_b64_e32 v[2:3], 0
	v_mov_b64_e32 v[4:5], 0
	v_mov_b64_e32 v[6:7], 0
	v_mov_b64_e32 v[8:9], 0
	v_mov_b64_e32 v[10:11], 0
	v_mov_b64_e32 v[12:13], 0
	v_mov_b64_e32 v[14:15], 0
	v_mov_b64_e32 v[16:17], 0
	v_mov_b64_e32 v[18:19], 0
	v_mov_b64_e32 v[20:21], 0
	v_mov_b64_e32 v[22:23], 0
	v_mov_b64_e32 v[24:25], 0
	v_mov_b64_e32 v[26:27], 0
	v_mov_b64_e32 v[28:29], 0
	v_mov_b64_e32 v[30:31], 0
	v_mov_b64_e32 v[32:33], 0
	v_mov_b64_e32 v[34:35], 0
	v_mov_b64_e32 v[36:37], 0
	v_mov_b64_e32 v[38:39], 0
	v_mov_b64_e32 v[40:41], 0
	v_mov_b64_e32 v[42:43], 0
	v_mov_b64_e32 v[44:45], 0
	v_mov_b64_e32 v[46:47], 0
	v_mov_b64_e32 v[48:49], 0
	v_mov_b64_e32 v[50:51], 0
	v_mov_b64_e32 v[52:53], 0
	v_mov_b64_e32 v[54:55], 0
	v_mov_b64_e32 v[56:57], 0
	v_mov_b64_e32 v[58:59], 0
	v_mov_b64_e32 v[60:61], 0
	v_mov_b64_e32 v[62:63], 0
	v_mov_b64_e32 v[64:65], 0
	v_mov_b64_e32 v[66:67], 0
	v_mov_b64_e32 v[68:69], 0
	v_mov_b64_e32 v[70:71], 0
	v_mov_b64_e32 v[72:73], 0
	v_mov_b64_e32 v[74:75], 0
	v_mov_b64_e32 v[76:77], 0
	v_mov_b64_e32 v[78:79], 0
	v_mov_b64_e32 v[80:81], 0
	v_mov_b64_e32 v[82:83], 0
	v_mov_b64_e32 v[84:85], 0
	v_mov_b64_e32 v[86:87], 0
	v_mov_b64_e32 v[88:89], 0
	v_mov_b64_e32 v[90:91], 0
	v_mov_b64_e32 v[92:93], 0
	v_mov_b64_e32 v[94:95], 0
	v_mov_b64_e32 v[96:97], 0
	v_mov_b64_e32 v[98:99], 0
	v_mov_b64_e32 v[100:101], 0
	v_mov_b64_e32 v[102:103], 0
	v_mov_b64_e32 v[104:105], 0
	v_mov_b64_e32 v[106:107], 0
	v_mov_b64_e32 v[108:109], 0
	v_mov_b64_e32 v[110:111], 0
	v_mov_b64_e32 v[112:113], 0
	v_mov_b64_e32 v[114:115], 0
	v_mov_b64_e32 v[116:117], 0
	v_mov_b64_e32 v[118:119], 0
	v_mov_b64_e32 v[120:121], 0
	v_mov_b64_e32 v[130:131], 0
	v_mov_b64_e32 v[132:133], 0
	v_mov_b64_e32 v[134:135], 0
	v_mov_b64_e32 v[136:137], 0
	s_waitcnt lgkmcnt(0)
	s_branch .LBB0_2079

.LBB0_2500:
	s_ashr_i32 s21, s20, 31
	s_lshl_b64 s[22:23], s[20:21], 19
	v_readlane_b32 s24, v254, 49
	v_readlane_b32 s25, v254, 50
	s_add_u32 s22, s24, s22
	s_addc_u32 s23, s25, s23
	s_and_b64 s[24:25], s[26:27], exec
	s_cselect_b32 s2, s23, s1
	s_cselect_b32 s21, s22, s0
	s_ashr_i32 s19, s18, 31
	s_lshl_b64 s[24:25], s[18:19], 19
	s_add_u32 s24, s4, s24
	s_addc_u32 s25, s5, s25
	s_and_b64 s[40:41], s[26:27], exec
	s_cselect_b32 s19, s25, s37
	s_cselect_b32 s66, s24, s36
	s_cmp_eq_u32 s38, 0
	s_cselect_b32 s67, -2, 0
	s_add_u32 s69, s36, 0x10000
	s_mov_b32 s68, 0
	s_addc_u32 s70, s37, 0
	v_lshl_add_u64 v[210:211], s[0:1], 0, v[204:205]
	v_lshl_add_u64 v[212:213], s[0:1], 0, v[206:207]
	v_mov_b64_e32 v[2:3], 0
	v_mov_b64_e32 v[4:5], 0
	v_mov_b64_e32 v[6:7], 0
	v_mov_b64_e32 v[8:9], 0
	v_mov_b64_e32 v[10:11], 0
	v_mov_b64_e32 v[12:13], 0
	v_mov_b64_e32 v[14:15], 0
	v_mov_b64_e32 v[16:17], 0
	v_mov_b64_e32 v[18:19], 0
	v_mov_b64_e32 v[20:21], 0
	v_mov_b64_e32 v[22:23], 0
	v_mov_b64_e32 v[24:25], 0
	v_mov_b64_e32 v[26:27], 0
	v_mov_b64_e32 v[28:29], 0
	v_mov_b64_e32 v[30:31], 0
	v_mov_b64_e32 v[32:33], 0
	v_mov_b64_e32 v[34:35], 0
	v_mov_b64_e32 v[36:37], 0
	v_mov_b64_e32 v[38:39], 0
	v_mov_b64_e32 v[40:41], 0
	v_mov_b64_e32 v[42:43], 0
	v_mov_b64_e32 v[44:45], 0
	v_mov_b64_e32 v[46:47], 0
	v_mov_b64_e32 v[48:49], 0
	v_mov_b64_e32 v[50:51], 0
	v_mov_b64_e32 v[52:53], 0
	v_mov_b64_e32 v[54:55], 0
	v_mov_b64_e32 v[56:57], 0
	v_mov_b64_e32 v[58:59], 0
	v_mov_b64_e32 v[60:61], 0
	v_mov_b64_e32 v[62:63], 0
	v_mov_b64_e32 v[64:65], 0
	v_mov_b64_e32 v[66:67], 0
	v_mov_b64_e32 v[68:69], 0
	v_mov_b64_e32 v[70:71], 0
	v_mov_b64_e32 v[72:73], 0
	v_mov_b64_e32 v[74:75], 0
	v_mov_b64_e32 v[76:77], 0
	v_mov_b64_e32 v[78:79], 0
	v_mov_b64_e32 v[80:81], 0
	v_mov_b64_e32 v[82:83], 0
	v_mov_b64_e32 v[84:85], 0
	v_mov_b64_e32 v[86:87], 0
	v_mov_b64_e32 v[88:89], 0
	v_mov_b64_e32 v[90:91], 0
	v_mov_b64_e32 v[92:93], 0
	v_mov_b64_e32 v[94:95], 0
	v_mov_b64_e32 v[96:97], 0
	v_mov_b64_e32 v[98:99], 0
	v_mov_b64_e32 v[100:101], 0
	v_mov_b64_e32 v[102:103], 0
	v_mov_b64_e32 v[104:105], 0
	v_mov_b64_e32 v[106:107], 0
	v_mov_b64_e32 v[108:109], 0
	v_mov_b64_e32 v[110:111], 0
	v_mov_b64_e32 v[112:113], 0
	v_mov_b64_e32 v[114:115], 0
	v_mov_b64_e32 v[116:117], 0
	v_mov_b64_e32 v[118:119], 0
	v_mov_b64_e32 v[120:121], 0
	v_mov_b64_e32 v[130:131], 0
	v_mov_b64_e32 v[132:133], 0
	v_mov_b64_e32 v[134:135], 0
	v_mov_b64_e32 v[136:137], 0
	s_branch .LBB0_2502

.LBB0_3525:
	s_ashr_i32 s21, s20, 31
	s_lshl_b64 s[22:23], s[20:21], 19
	s_add_u32 s22, s33, s22
	s_addc_u32 s23, s42, s23
	s_and_b64 s[24:25], s[0:1], exec
	s_cselect_b32 s21, s23, s29
	s_cselect_b32 s64, s22, s28
	s_ashr_i32 s19, s18, 31
	s_lshl_b64 s[24:25], s[18:19], 19
	s_add_u32 s24, s43, s24
	s_addc_u32 s25, s44, s25
	s_and_b64 s[36:37], s[0:1], exec
	s_cselect_b32 s19, s25, s31
	s_cselect_b32 s65, s24, s30
	s_cmp_eq_u32 s34, 0
	s_cselect_b32 s66, -2, 0
	s_add_u32 s68, s30, 0x10000
	v_mov_b32_e32 v66, 0
	s_mov_b32 s67, 0
	s_addc_u32 s69, s31, 0
	v_lshl_add_u64 v[210:211], s[28:29], 0, v[202:203]
	v_lshl_add_u64 v[212:213], s[28:29], 0, v[204:205]
	s_mov_b64 s[30:31], 0
	v_mov_b32_e32 v67, 0
	v_mov_b64_e32 v[68:69], 0
	v_mov_b64_e32 v[70:71], 0
	v_mov_b64_e32 v[72:73], 0
	v_mov_b64_e32 v[74:75], 0
	v_mov_b64_e32 v[76:77], 0
	s_waitcnt lgkmcnt(0)
	v_mov_b64_e32 v[78:79], 0
	v_mov_b64_e32 v[80:81], 0
	v_mov_b64_e32 v[82:83], 0
	v_mov_b64_e32 v[84:85], 0
	v_mov_b64_e32 v[86:87], 0
	v_mov_b64_e32 v[88:89], 0
	v_mov_b64_e32 v[90:91], 0
	v_mov_b64_e32 v[92:93], 0
	v_mov_b64_e32 v[94:95], 0
	v_mov_b64_e32 v[96:97], 0
	v_mov_b64_e32 v[98:99], 0
	v_mov_b64_e32 v[100:101], 0
	v_mov_b64_e32 v[102:103], 0
	v_mov_b64_e32 v[104:105], 0
	v_mov_b64_e32 v[106:107], 0
	v_mov_b64_e32 v[108:109], 0
	v_mov_b64_e32 v[110:111], 0
	v_mov_b64_e32 v[112:113], 0
	v_mov_b64_e32 v[114:115], 0
	v_mov_b64_e32 v[116:117], 0
	v_mov_b64_e32 v[118:119], 0
	v_mov_b64_e32 v[120:121], 0
	v_mov_b64_e32 v[122:123], 0
	v_mov_b64_e32 v[124:125], 0
	v_mov_b64_e32 v[126:127], 0
	v_mov_b64_e32 v[128:129], 0
	v_mov_b64_e32 v[130:131], 0
	v_mov_b64_e32 v[132:133], 0
	v_mov_b64_e32 v[134:135], 0
	v_mov_b64_e32 v[136:137], 0
	v_mov_b64_e32 v[138:139], 0
	v_mov_b64_e32 v[140:141], 0
	v_mov_b64_e32 v[142:143], 0
	v_mov_b64_e32 v[144:145], 0
	v_mov_b64_e32 v[146:147], 0
	v_mov_b64_e32 v[148:149], 0
	v_mov_b64_e32 v[150:151], 0
	v_mov_b64_e32 v[152:153], 0
	v_mov_b64_e32 v[154:155], 0
	v_mov_b64_e32 v[156:157], 0
	v_mov_b64_e32 v[158:159], 0
	v_mov_b64_e32 v[160:161], 0
	v_mov_b64_e32 v[162:163], 0
	v_mov_b64_e32 v[164:165], 0
	v_mov_b64_e32 v[166:167], 0
	v_mov_b64_e32 v[168:169], 0
	v_mov_b64_e32 v[170:171], 0
	v_mov_b64_e32 v[172:173], 0
	v_mov_b64_e32 v[174:175], 0
	v_mov_b64_e32 v[176:177], 0
	v_mov_b64_e32 v[178:179], 0
	v_mov_b64_e32 v[180:181], 0
	v_mov_b64_e32 v[182:183], 0
	v_mov_b64_e32 v[184:185], 0
	v_mov_b64_e32 v[186:187], 0
	v_mov_b64_e32 v[188:189], 0
	v_mov_b64_e32 v[190:191], 0
	v_mov_b64_e32 v[192:193], 0
	s_branch .LBB0_3527

.LBB0_3829:
	s_ashr_i32 s17, s16, 31
	s_lshl_b64 s[20:21], s[16:17], 19
	s_add_u32 s20, s39, s20
	s_addc_u32 s21, s40, s21
	s_and_b64 s[4:5], s[4:5], exec
	s_cselect_b32 s15, s21, s27
	s_cselect_b32 s17, s20, s26
	s_cmp_eq_u32 s30, 0
	s_cselect_b32 s67, -2, 0
	s_add_u32 s69, s28, 0x10000
	s_mov_b32 s68, 0
	s_addc_u32 s70, s29, 0
	v_lshl_add_u64 v[238:239], s[26:27], 0, v[216:217]
	v_lshl_add_u64 v[240:241], s[26:27], 0, v[218:219]
	s_mov_b64 s[4:5], 0
	v_mov_b64_e32 v[2:3], 0
	v_mov_b64_e32 v[4:5], 0
	v_mov_b64_e32 v[6:7], 0
	v_mov_b64_e32 v[8:9], 0
	v_mov_b64_e32 v[10:11], 0
	v_mov_b64_e32 v[12:13], 0
	v_mov_b64_e32 v[14:15], 0
	v_mov_b64_e32 v[16:17], 0
	v_mov_b64_e32 v[18:19], 0
	v_mov_b64_e32 v[20:21], 0
	v_mov_b64_e32 v[22:23], 0
	v_mov_b64_e32 v[24:25], 0
	v_mov_b64_e32 v[26:27], 0
	v_mov_b64_e32 v[28:29], 0
	v_mov_b64_e32 v[30:31], 0
	v_mov_b64_e32 v[32:33], 0
	v_mov_b64_e32 v[34:35], 0
	v_mov_b64_e32 v[36:37], 0
	v_mov_b64_e32 v[38:39], 0
	v_mov_b64_e32 v[40:41], 0
	v_mov_b64_e32 v[42:43], 0
	v_mov_b64_e32 v[44:45], 0
	v_mov_b64_e32 v[46:47], 0
	v_mov_b64_e32 v[48:49], 0
	v_mov_b64_e32 v[50:51], 0
	v_mov_b64_e32 v[52:53], 0
	v_mov_b64_e32 v[54:55], 0
	v_mov_b64_e32 v[56:57], 0
	v_mov_b64_e32 v[58:59], 0
	v_mov_b64_e32 v[60:61], 0
	v_mov_b64_e32 v[62:63], 0
	v_mov_b64_e32 v[64:65], 0
	v_mov_b64_e32 v[66:67], 0
	v_mov_b64_e32 v[68:69], 0
	v_mov_b64_e32 v[70:71], 0
	v_mov_b64_e32 v[72:73], 0
	v_mov_b64_e32 v[74:75], 0
	v_mov_b64_e32 v[76:77], 0
	v_mov_b64_e32 v[78:79], 0
	v_mov_b64_e32 v[80:81], 0
	v_mov_b64_e32 v[82:83], 0
	v_mov_b64_e32 v[84:85], 0
	v_mov_b64_e32 v[86:87], 0
	v_mov_b64_e32 v[88:89], 0
	v_mov_b64_e32 v[90:91], 0
	v_mov_b64_e32 v[92:93], 0
	v_mov_b64_e32 v[94:95], 0
	v_mov_b64_e32 v[96:97], 0
	v_mov_b64_e32 v[98:99], 0
	v_mov_b64_e32 v[100:101], 0
	v_mov_b64_e32 v[102:103], 0
	v_mov_b64_e32 v[104:105], 0
	v_mov_b64_e32 v[106:107], 0
	v_mov_b64_e32 v[108:109], 0
	v_mov_b64_e32 v[110:111], 0
	v_mov_b64_e32 v[112:113], 0
	v_mov_b64_e32 v[114:115], 0
	v_mov_b64_e32 v[116:117], 0
	v_mov_b64_e32 v[118:119], 0
	v_mov_b64_e32 v[120:121], 0
	v_mov_b64_e32 v[122:123], 0
	v_mov_b64_e32 v[124:125], 0
	v_mov_b64_e32 v[126:127], 0
	v_mov_b64_e32 v[128:129], 0
	s_cmp_eq_u32 s22, s64
	s_cbranch_scc1 .Lp15_rs
	v_lshl_add_u32 v130, s22, 8, v1
	v_readlane_b32 s98, v254, 47
	v_ashrrev_i32_e32 v131, 31, v130
	v_readlane_b32 s99, v254, 48
	s_mov_b32 s64, s22
	s_nop 0
	v_lshl_add_u64 v[130:131], v[130:131], 2, s[98:99]
	global_load_dword v236, v[130:131], off offset:704
	global_load_dword v234, v[130:131], off offset:640
	global_load_dword v232, v[130:131], off offset:576
	global_load_dword v230, v[130:131], off offset:512
	global_load_dword v228, v[130:131], off offset:192
	global_load_dword v226, v[130:131], off offset:128
	global_load_dword v224, v[130:131], off offset:64
	global_load_dword v222, v[130:131], off

.LBB0_3924:
	s_cmp_eq_u32 s30, 0
	s_cselect_b32 s71, -2, 0
	s_add_u32 s73, s28, 0x10000
	v_mov_b32_e32 v66, 0
	s_mov_b32 s72, 0
	s_addc_u32 s74, s29, 0
	v_lshl_add_u64 v[210:211], s[26:27], 0, v[202:203]
	v_lshl_add_u64 v[212:213], s[26:27], 0, v[204:205]
	s_mov_b64 s[28:29], 0
	v_mov_b32_e32 v67, 0
	v_mov_b64_e32 v[68:69], 0
	v_mov_b64_e32 v[70:71], 0
	v_mov_b64_e32 v[72:73], 0
	v_mov_b64_e32 v[74:75], 0
	v_mov_b64_e32 v[76:77], 0
	v_mov_b64_e32 v[78:79], 0
	v_mov_b64_e32 v[80:81], 0
	v_mov_b64_e32 v[82:83], 0
	v_mov_b64_e32 v[84:85], 0
	v_mov_b64_e32 v[86:87], 0
	v_mov_b64_e32 v[88:89], 0
	v_mov_b64_e32 v[90:91], 0
	v_mov_b64_e32 v[92:93], 0
	v_mov_b64_e32 v[94:95], 0
	v_mov_b64_e32 v[96:97], 0
	v_mov_b64_e32 v[98:99], 0
	v_mov_b64_e32 v[100:101], 0
	v_mov_b64_e32 v[102:103], 0
	v_mov_b64_e32 v[104:105], 0
	v_mov_b64_e32 v[106:107], 0
	v_mov_b64_e32 v[108:109], 0
	v_mov_b64_e32 v[110:111], 0
	v_mov_b64_e32 v[112:113], 0
	v_mov_b64_e32 v[114:115], 0
	v_mov_b64_e32 v[116:117], 0
	v_mov_b64_e32 v[118:119], 0
	v_mov_b64_e32 v[120:121], 0
	v_mov_b64_e32 v[122:123], 0
	v_mov_b64_e32 v[124:125], 0
	v_mov_b64_e32 v[126:127], 0
	v_mov_b64_e32 v[128:129], 0
	v_mov_b64_e32 v[130:131], 0
	v_mov_b64_e32 v[132:133], 0
	v_mov_b64_e32 v[134:135], 0
	v_mov_b64_e32 v[136:137], 0
	v_mov_b64_e32 v[138:139], 0
	v_mov_b64_e32 v[140:141], 0
	v_mov_b64_e32 v[142:143], 0
	v_mov_b64_e32 v[144:145], 0
	v_mov_b64_e32 v[146:147], 0
	v_mov_b64_e32 v[148:149], 0
	v_mov_b64_e32 v[150:151], 0
	v_mov_b64_e32 v[152:153], 0
	v_mov_b64_e32 v[154:155], 0
	v_mov_b64_e32 v[156:157], 0
	v_mov_b64_e32 v[158:159], 0
	v_mov_b64_e32 v[160:161], 0
	v_mov_b64_e32 v[162:163], 0
	v_mov_b64_e32 v[164:165], 0
	v_mov_b64_e32 v[166:167], 0
	v_mov_b64_e32 v[168:169], 0
	v_mov_b64_e32 v[170:171], 0
	v_mov_b64_e32 v[172:173], 0
	v_mov_b64_e32 v[174:175], 0
	v_mov_b64_e32 v[176:177], 0
	v_mov_b64_e32 v[178:179], 0
	v_mov_b64_e32 v[180:181], 0
	v_mov_b64_e32 v[182:183], 0
	v_mov_b64_e32 v[184:185], 0
	v_mov_b64_e32 v[186:187], 0
	v_mov_b64_e32 v[188:189], 0
	v_mov_b64_e32 v[190:191], 0
	v_mov_b64_e32 v[192:193], 0
	s_branch .LBB0_3926

.LBB0_3947:
	s_lshl_b32 s8, s8, 5
	s_and_b32 s26, s8, 0x60
	v_lshl_or_b32 v3, s9, 13, v219
	v_lshlrev_b32_e32 v4, 1, v248
	s_lshr_b32 s8, s26, 3
	v_lshlrev_b32_e32 v2, 6, v248
	v_and_b32_e32 v4, 16, v4
	v_or_b32_e32 v5, v3, v218
	v_or_b32_e32 v6, s8, v215
	s_add_u32 s8, s0, 0x8000
	v_lshl_or_b32 v202, s9, 6, v248
	v_or3_b32 v5, v5, v2, v4
	v_bitop3_b32 v2, v2, v4, v217 bitop3:0x36
	s_addc_u32 s9, s1, 0
	v_or_b32_e32 v4, v2, v3
	s_add_i32 m0, s20, 0x18000
	v_lshl_add_u64 v[2:3], s[8:9], 0, v[196:197]
	s_waitcnt vmcnt(2)
	s_barrier
	global_load_lds_dwordx4 v[2:3], off
	s_add_i32 m0, s20, 0x1a000
	v_lshl_add_u64 v[2:3], s[8:9], 0, v[200:201]
	s_add_u32 s8, s4, 0x8000
	s_addc_u32 s9, s5, 0
	s_add_i32 s30, s20, 0x8000
	global_load_lds_dwordx4 v[2:3], off
	v_lshl_add_u64 v[2:3], s[8:9], 0, v[194:195]
	s_mov_b32 m0, s30
	s_add_i32 s31, s20, 0xa000
	global_load_lds_dwordx4 v[2:3], off
	v_lshl_add_u64 v[2:3], s[8:9], 0, v[198:199]
	s_add_u32 s8, s0, 0x9000
	s_mov_b32 m0, s31
	s_addc_u32 s9, s1, 0
	global_load_lds_dwordx4 v[2:3], off
	s_add_i32 m0, s20, 0x1c000
	v_lshl_add_u64 v[2:3], s[8:9], 0, v[196:197]
	global_load_lds_dwordx4 v[2:3], off
	v_lshl_add_u64 v[2:3], s[8:9], 0, v[200:201]
	s_add_i32 m0, s20, 0x1e000
	s_mul_hi_i32 s8, s10, 0x1c0000
	global_load_lds_dwordx4 v[2:3], off
	s_mul_i32 s10, s10, 0x1c0000
	v_lshlrev_b32_e32 v3, 12, v0
	v_lshlrev_b32_e32 v6, 10, v6
	s_add_u32 s6, s10, s6
	v_lshlrev_b32_e32 v2, 8, v0
	v_and_b32_e32 v3, 0x2000, v3
	v_or_b32_e32 v203, v216, v6
	v_or_b32_e32 v208, v6, v220
	s_addc_u32 s7, s8, s7
	v_and_or_b32 v6, v2, s12, v3
	s_movk_i32 s8, 0x600
	v_lshlrev_b32_e32 v2, 2, v0
	v_bfe_u32 v3, v0, 2, 4
	v_and_or_b32 v2, v2, s8, v6
	v_lshlrev_b32_e32 v7, 5, v3
	s_add_u32 s6, s96, s6
	v_or3_b32 v2, v2, v7, v1
	v_mov_b32_e32 v3, v197
	s_addc_u32 s7, s97, s7
	v_lshl_add_u64 v[204:205], s[6:7], 0, v[2:3]
	v_lshrrev_b32_e32 v2, 2, v214
	s_movk_i32 s8, 0xe00
	s_waitcnt vmcnt(6)
	v_and_or_b32 v2, v2, s8, v6
	s_add_i32 s8, 0, 0x10000
	s_add_i32 s38, 0, 0x18000
	s_add_i32 s39, 0, 0x1c000
	v_or3_b32 v2, v2, v7, v1
	v_add_u32_e32 v1, s8, v203
	v_add_u32_e32 v209, s8, v208
	s_add_i32 s8, 0, 0x14000
	s_add_i32 s40, s38, s11
	s_add_i32 s42, s39, s11
	s_mov_b32 s34, -2
	v_lshl_add_u64 v[206:207], s[6:7], 0, v[2:3]
	s_lshl_b32 s35, s19, 15
	s_mov_b64 s[6:7], 0x10000
	v_add_u32_e32 v210, s8, v203
	v_add_u32_e32 v211, s8, v208
	v_add_u32_e32 v212, 0, v5
	v_add_u32_e32 v213, 0, v4
	s_mov_b64 s[8:9], 0x551f9000
	s_add_i32 s36, s20, 0xc000
	s_add_i32 s37, s20, 0xe000
	v_mov_b32_e32 v214, 0x7f7f7f7f
	s_add_i32 s41, s40, 0x2000
	s_add_i32 s43, s42, 0x2000
	v_mov_b64_e32 v[66:67], 0
	v_mov_b64_e32 v[68:69], 0
	v_mov_b64_e32 v[70:71], 0
	v_mov_b64_e32 v[72:73], 0
	v_mov_b64_e32 v[74:75], 0
	v_mov_b64_e32 v[76:77], 0
	v_mov_b64_e32 v[78:79], 0
	v_mov_b64_e32 v[80:81], 0
	v_mov_b64_e32 v[82:83], 0
	v_mov_b64_e32 v[84:85], 0
	v_mov_b64_e32 v[86:87], 0
	v_mov_b64_e32 v[88:89], 0
	v_mov_b64_e32 v[90:91], 0
	v_mov_b64_e32 v[92:93], 0
	v_mov_b64_e32 v[94:95], 0
	v_mov_b64_e32 v[96:97], 0
	v_mov_b64_e32 v[98:99], 0
	v_mov_b64_e32 v[100:101], 0
	v_mov_b64_e32 v[102:103], 0
	v_mov_b64_e32 v[104:105], 0
	v_mov_b64_e32 v[106:107], 0
	v_mov_b64_e32 v[108:109], 0
	v_mov_b64_e32 v[110:111], 0
	v_mov_b64_e32 v[112:113], 0
	v_mov_b64_e32 v[114:115], 0
	v_mov_b64_e32 v[116:117], 0
	v_mov_b64_e32 v[118:119], 0
	v_mov_b64_e32 v[120:121], 0
	v_mov_b64_e32 v[122:123], 0
	v_mov_b64_e32 v[124:125], 0
	v_mov_b64_e32 v[126:127], 0
	v_mov_b64_e32 v[128:129], 0
	v_mov_b64_e32 v[130:131], 0
	v_mov_b64_e32 v[132:133], 0
	v_mov_b64_e32 v[134:135], 0
	v_mov_b64_e32 v[136:137], 0
	v_mov_b64_e32 v[138:139], 0
	v_mov_b64_e32 v[140:141], 0
	v_mov_b64_e32 v[142:143], 0
	v_mov_b64_e32 v[144:145], 0
	v_mov_b64_e32 v[146:147], 0
	v_mov_b64_e32 v[148:149], 0
	v_mov_b64_e32 v[150:151], 0
	v_mov_b64_e32 v[152:153], 0
	v_mov_b64_e32 v[154:155], 0
	v_mov_b64_e32 v[156:157], 0
	v_mov_b64_e32 v[158:159], 0
	v_mov_b64_e32 v[160:161], 0
	v_mov_b64_e32 v[162:163], 0
	v_mov_b64_e32 v[164:165], 0
	v_mov_b64_e32 v[166:167], 0
	v_mov_b64_e32 v[168:169], 0
	v_mov_b64_e32 v[170:171], 0
	v_mov_b64_e32 v[172:173], 0
	v_mov_b64_e32 v[174:175], 0
	v_mov_b64_e32 v[176:177], 0
	v_mov_b64_e32 v[178:179], 0
	v_mov_b64_e32 v[180:181], 0
	v_mov_b64_e32 v[182:183], 0
	v_mov_b64_e32 v[184:185], 0
	v_mov_b64_e32 v[186:187], 0
	v_mov_b64_e32 v[188:189], 0
	v_mov_b64_e32 v[190:191], 0
	v_mov_b64_e32 v[192:193], 0
	s_barrier
	s_branch .LBB0_3949
